# wt2: bulk 16-byte stores of the barrier-terminated phases (IN, conv, attention, G2, combine) made write-through (sc1) so the barrier's L2 write-back finds a clean L2; on top of rt1
# speedup vs baseline: 1.0009x; 1.0009x over previous
; #define EFENCE() asm volatile("" ::: "memory")
;     __device__ __forceinline__ bool operator()(f32x4 (&acc)[2][2][4][2], const pg8::Unit& u, int wr, int wc, int fr, int fq) const {
;     ...
;         if (pn < 8) {
;             bf16_t* dst = pn < 4 ? Q : Kb; const float sc = pn < 4 ? QSCALE : 1.0f; const int colb = (pn & 3) * 256 + wc * 32 + 8 * fq;
;             const bool rot = ((wc & 1) == 0) && (fq < 2);
; #pragma unroll
;             for (int ai = 0; ai < 2; ++ai)
; #pragma unroll
;               for (int mh = 0; mh < 2; ++mh) {
;                 f32x4 c4[2], s4[2];
; #pragma unroll
;                 for (int q = 0; q < 2; ++q) { c4[q] = (f32x4){1.f, 1.f, 1.f, 1.f}; s4[q] = (f32x4){0.f, 0.f, 0.f, 0.f};
;                     if (rot) { const int t = (row0 + ai * 128 + (2 * mh + q) * 16) & (SEQ - 1); c4[q] = *(const f32x4*)(cosT + t * 8 + 4 * fq); s4[q] = *(const f32x4*)(sinT + t * 8 + 4 * fq); } }
; #pragma unroll
;                 for (int q = 0; q < 2; ++q) { const int m = 2 * mh + q; const int row = row0 + ai * 128 + m * 16; const float rsv = RS_AT(ai, m);
; #pragma unroll
;                     for (int bj = 0; bj < 2; ++bj) { f32x4 x1 = acc[ai][bj][m][0] * rsv, x2 = acc[ai][bj][m][1] * rsv;
;                         const f32x4 y1 = x1 * c4[q] - x2 * s4[q], y2 = x2 * c4[q] + x1 * s4[q];
;                         if (rot) { x1 = y1; x2 = y2; }
;                         st8(dst + (size_t)row * DM + colb + bj * 128, x1 * sc, x2 * sc); } }
;                 EFENCE(); }
.Lrot_741:
	s_or_b64 exec, exec, s[4:5]
	s_cmp_lt_i32 s29, 4
	s_cselect_b64 vcc, -1, 0
	s_and_b64 s[2:3], vcc, exec
	v_readlane_b32 s2, v252, 16
	v_readlane_b32 s3, v252, 17
	v_readlane_b32 s4, v251, 43
	s_cselect_b32 s3, s3, s4
	v_readlane_b32 s4, v251, 42
	s_cselect_b32 s2, s2, s4
	s_lshl_b32 s4, s29, 8
	v_pk_mul_f32 v[122:123], v[122:123], v[198:199] op_sel_hi:[1,0]
	v_pk_mul_f32 v[120:121], v[120:121], v[198:199] op_sel_hi:[1,0]
	v_mov_b32_e32 v129, 0x3e38aa3b
	s_and_b32 s4, s4, 0x300
	v_pk_mul_f32 v[126:127], v[126:127], v[198:199] op_sel_hi:[1,0]
	v_pk_mul_f32 v[124:125], v[124:125], v[198:199] op_sel_hi:[1,0]
	s_waitcnt vmcnt(5)
	v_pk_mul_f32 v[192:193], v[122:123], v[140:141]
	v_pk_mul_f32 v[208:209], v[120:121], v[138:139]
	v_cndmask_b32_e32 v204, 1.0, v129, vcc
	v_or_b32_e32 v129, s4, v203
	s_waitcnt vmcnt(0)
	v_pk_fma_f32 v[192:193], v[126:127], v[144:145], v[192:193]
	v_pk_fma_f32 v[208:209], v[124:125], v[142:143], v[208:209]
	v_pk_mul_f32 v[210:211], v[122:123], v[144:145]
	v_pk_mul_f32 v[216:217], v[120:121], v[142:143]
	v_lshlrev_b32_e32 v160, 1, v129
	v_pk_fma_f32 v[210:211], v[126:127], v[140:141], v[210:211] neg_lo:[0,0,1] neg_hi:[0,0,1]
	v_pk_fma_f32 v[216:217], v[124:125], v[138:139], v[216:217] neg_lo:[0,0,1] neg_hi:[0,0,1]
	v_cndmask_b32_e64 v123, v123, v193, s[0:1]
	v_cndmask_b32_e64 v122, v122, v192, s[0:1]
	v_cndmask_b32_e64 v121, v121, v209, s[0:1]
	v_cndmask_b32_e64 v120, v120, v208, s[0:1]
	v_lshl_add_u64 v[206:207], s[2:3], 0, v[160:161]
	v_lshlrev_b64 v[190:191], 11, v[184:185]
	v_cndmask_b32_e64 v127, v127, v211, s[0:1]
	v_cndmask_b32_e64 v126, v126, v210, s[0:1]
	v_cndmask_b32_e64 v125, v125, v217, s[0:1]
	v_cndmask_b32_e64 v124, v124, v216, s[0:1]
	v_pk_mul_f32 v[192:193], v[204:205], v[122:123] op_sel_hi:[0,1]
	v_pk_mul_f32 v[122:123], v[204:205], v[120:121] op_sel_hi:[0,1]
	v_lshl_add_u64 v[190:191], v[206:207], 0, v[190:191]
	v_pk_mul_f32 v[126:127], v[204:205], v[126:127] op_sel_hi:[0,1]
	v_pk_mul_f32 v[124:125], v[204:205], v[124:125] op_sel_hi:[0,1]
	v_cvt_pk_bf16_f32 v120, v124, v125
	v_cvt_pk_bf16_f32 v121, v126, v127
	v_cvt_pk_bf16_f32 v122, v122, v123
	v_cvt_pk_bf16_f32 v123, v192, v193
	v_pk_mul_f32 v[114:115], v[114:115], v[198:199] op_sel_hi:[1,0]
	v_pk_mul_f32 v[112:113], v[112:113], v[198:199] op_sel_hi:[1,0]
	global_store_dwordx4 v[190:191], v[120:123], off sc1
	v_pk_mul_f32 v[118:119], v[118:119], v[198:199] op_sel_hi:[1,0]
	v_pk_mul_f32 v[116:117], v[116:117], v[198:199] op_sel_hi:[1,0]
	v_pk_mul_f32 v[120:121], v[114:115], v[140:141]
	v_pk_mul_f32 v[122:123], v[112:113], v[138:139]
	v_pk_fma_f32 v[120:121], v[118:119], v[144:145], v[120:121]
	v_pk_fma_f32 v[122:123], v[116:117], v[142:143], v[122:123]
	v_pk_mul_f32 v[124:125], v[114:115], v[144:145]
	v_pk_mul_f32 v[126:127], v[112:113], v[142:143]
	v_pk_fma_f32 v[124:125], v[118:119], v[140:141], v[124:125] neg_lo:[0,0,1] neg_hi:[0,0,1]
	v_pk_fma_f32 v[126:127], v[116:117], v[138:139], v[126:127] neg_lo:[0,0,1] neg_hi:[0,0,1]
	v_cndmask_b32_e64 v115, v115, v121, s[0:1]
	v_cndmask_b32_e64 v114, v114, v120, s[0:1]
	v_cndmask_b32_e64 v113, v113, v123, s[0:1]
	v_cndmask_b32_e64 v112, v112, v122, s[0:1]
	v_cndmask_b32_e64 v119, v119, v125, s[0:1]
	v_cndmask_b32_e64 v118, v118, v124, s[0:1]
	v_cndmask_b32_e64 v117, v117, v127, s[0:1]
	v_cndmask_b32_e64 v116, v116, v126, s[0:1]
	v_pk_mul_f32 v[120:121], v[204:205], v[114:115] op_sel_hi:[0,1]
	v_pk_mul_f32 v[114:115], v[204:205], v[112:113] op_sel_hi:[0,1]
	v_pk_mul_f32 v[118:119], v[204:205], v[118:119] op_sel_hi:[0,1]
	v_pk_mul_f32 v[116:117], v[204:205], v[116:117] op_sel_hi:[0,1]
	v_cvt_pk_bf16_f32 v112, v116, v117
	v_cvt_pk_bf16_f32 v113, v118, v119
	v_cvt_pk_bf16_f32 v114, v114, v115
	v_cvt_pk_bf16_f32 v115, v120, v121
	v_pk_mul_f32 v[106:107], v[106:107], v[154:155] op_sel_hi:[1,0]
	v_pk_mul_f32 v[104:105], v[104:105], v[154:155] op_sel_hi:[1,0]
	global_store_dwordx4 v[190:191], v[112:115], off offset:256 sc1
	v_pk_mul_f32 v[110:111], v[110:111], v[154:155] op_sel_hi:[1,0]
	v_pk_mul_f32 v[108:109], v[108:109], v[154:155] op_sel_hi:[1,0]
	v_pk_mul_f32 v[114:115], v[104:105], v[130:131]
	v_pk_mul_f32 v[116:117], v[106:107], v[132:133]
	v_pk_fma_f32 v[114:115], v[108:109], v[134:135], v[114:115]
	v_pk_fma_f32 v[116:117], v[110:111], v[136:137], v[116:117]
	v_pk_mul_f32 v[118:119], v[104:105], v[134:135]
	v_pk_mul_f32 v[120:121], v[106:107], v[136:137]
	v_pk_fma_f32 v[118:119], v[108:109], v[130:131], v[118:119] neg_lo:[0,0,1] neg_hi:[0,0,1]
	v_pk_fma_f32 v[120:121], v[110:111], v[132:133], v[120:121] neg_lo:[0,0,1] neg_hi:[0,0,1]
	v_cndmask_b32_e64 v107, v107, v117, s[0:1]
	v_cndmask_b32_e64 v106, v106, v116, s[0:1]
	v_cndmask_b32_e64 v105, v105, v115, s[0:1]
	v_cndmask_b32_e64 v104, v104, v114, s[0:1]
	v_lshlrev_b64 v[112:113], 11, v[196:197]
	v_cndmask_b32_e64 v111, v111, v121, s[0:1]
	v_cndmask_b32_e64 v110, v110, v120, s[0:1]
	v_cndmask_b32_e64 v109, v109, v119, s[0:1]
	v_cndmask_b32_e64 v108, v108, v118, s[0:1]
	v_pk_mul_f32 v[114:115], v[204:205], v[106:107] op_sel_hi:[0,1]
	v_pk_mul_f32 v[106:107], v[204:205], v[104:105] op_sel_hi:[0,1]
	v_lshl_add_u64 v[112:113], v[206:207], 0, v[112:113]
	v_pk_mul_f32 v[110:111], v[204:205], v[110:111] op_sel_hi:[0,1]
	v_pk_mul_f32 v[108:109], v[204:205], v[108:109] op_sel_hi:[0,1]
	v_cvt_pk_bf16_f32 v104, v108, v109
	v_cvt_pk_bf16_f32 v105, v110, v111
	v_cvt_pk_bf16_f32 v106, v106, v107
	v_cvt_pk_bf16_f32 v107, v114, v115
	v_pk_mul_f32 v[98:99], v[98:99], v[154:155] op_sel_hi:[1,0]
	v_pk_mul_f32 v[96:97], v[96:97], v[154:155] op_sel_hi:[1,0]
	global_store_dwordx4 v[112:113], v[104:107], off sc1
	v_pk_mul_f32 v[102:103], v[102:103], v[154:155] op_sel_hi:[1,0]
; #define EFENCE() asm volatile("" ::: "memory")
;     __device__ __forceinline__ bool operator()(f32x4 (&acc)[2][2][4][2], const pg8::Unit& u, int wr, int wc, int fr, int fq) const {
;     ...
;         if (pn < 8) {
;             bf16_t* dst = pn < 4 ? Q : Kb; const float sc = pn < 4 ? QSCALE : 1.0f; const int colb = (pn & 3) * 256 + wc * 32 + 8 * fq;
;             const bool rot = ((wc & 1) == 0) && (fq < 2);
; #pragma unroll
;             for (int ai = 0; ai < 2; ++ai)
; #pragma unroll
;               for (int mh = 0; mh < 2; ++mh) {
;                 f32x4 c4[2], s4[2];
; #pragma unroll
;                 for (int q = 0; q < 2; ++q) { c4[q] = (f32x4){1.f, 1.f, 1.f, 1.f}; s4[q] = (f32x4){0.f, 0.f, 0.f, 0.f};
;                     if (rot) { const int t = (row0 + ai * 128 + (2 * mh + q) * 16) & (SEQ - 1); c4[q] = *(const f32x4*)(cosT + t * 8 + 4 * fq); s4[q] = *(const f32x4*)(sinT + t * 8 + 4 * fq); } }
; #pragma unroll
;                 for (int q = 0; q < 2; ++q) { const int m = 2 * mh + q; const int row = row0 + ai * 128 + m * 16; const float rsv = RS_AT(ai, m);
; #pragma unroll
;                     for (int bj = 0; bj < 2; ++bj) { f32x4 x1 = acc[ai][bj][m][0] * rsv, x2 = acc[ai][bj][m][1] * rsv;
;                         const f32x4 y1 = x1 * c4[q] - x2 * s4[q], y2 = x2 * c4[q] + x1 * s4[q];
;                         if (rot) { x1 = y1; x2 = y2; }
;                         st8(dst + (size_t)row * DM + colb + bj * 128, x1 * sc, x2 * sc); } }
;                 EFENCE(); }
	v_pk_mul_f32 v[100:101], v[100:101], v[154:155] op_sel_hi:[1,0]
	v_pk_mul_f32 v[104:105], v[96:97], v[130:131]
	v_pk_mul_f32 v[106:107], v[98:99], v[132:133]
	v_pk_fma_f32 v[104:105], v[100:101], v[134:135], v[104:105]
	v_pk_fma_f32 v[106:107], v[102:103], v[136:137], v[106:107]
	v_pk_mul_f32 v[108:109], v[96:97], v[134:135]
	v_pk_mul_f32 v[110:111], v[98:99], v[136:137]
	v_pk_fma_f32 v[108:109], v[100:101], v[130:131], v[108:109] neg_lo:[0,0,1] neg_hi:[0,0,1]
	v_pk_fma_f32 v[110:111], v[102:103], v[132:133], v[110:111] neg_lo:[0,0,1] neg_hi:[0,0,1]
	v_cndmask_b32_e64 v99, v99, v107, s[0:1]
	v_cndmask_b32_e64 v98, v98, v106, s[0:1]
	v_cndmask_b32_e64 v97, v97, v105, s[0:1]
	v_cndmask_b32_e64 v96, v96, v104, s[0:1]
	v_cndmask_b32_e64 v103, v103, v111, s[0:1]
	v_cndmask_b32_e64 v102, v102, v110, s[0:1]
	v_cndmask_b32_e64 v101, v101, v109, s[0:1]
	v_cndmask_b32_e64 v100, v100, v108, s[0:1]
	v_pk_mul_f32 v[104:105], v[204:205], v[98:99] op_sel_hi:[0,1]
	v_pk_mul_f32 v[98:99], v[204:205], v[96:97] op_sel_hi:[0,1]
	v_pk_mul_f32 v[102:103], v[204:205], v[102:103] op_sel_hi:[0,1]
	v_pk_mul_f32 v[100:101], v[204:205], v[100:101] op_sel_hi:[0,1]
	v_cvt_pk_bf16_f32 v96, v100, v101
	v_cvt_pk_bf16_f32 v97, v102, v103
	v_cvt_pk_bf16_f32 v98, v98, v99
	v_cvt_pk_bf16_f32 v99, v104, v105
	global_store_dwordx4 v[112:113], v[96:99], off offset:256 sc1
	v_pk_mul_f32 v[90:91], v[90:91], v[202:203] op_sel_hi:[1,0]
	v_pk_mul_f32 v[88:89], v[88:89], v[202:203] op_sel_hi:[1,0]
	v_pk_mul_f32 v[94:95], v[94:95], v[202:203] op_sel_hi:[1,0]
	v_pk_mul_f32 v[92:93], v[92:93], v[202:203] op_sel_hi:[1,0]
	v_pk_mul_f32 v[110:111], v[90:91], v[222:223]
	v_pk_mul_f32 v[112:113], v[88:89], v[220:221]
	v_pk_fma_f32 v[110:111], v[94:95], v[226:227], v[110:111]
	v_pk_fma_f32 v[112:113], v[92:93], v[224:225], v[112:113]
	v_pk_mul_f32 v[114:115], v[90:91], v[226:227]
	v_pk_mul_f32 v[116:117], v[88:89], v[224:225]
	v_mov_b32_e32 v205, v204
	v_pk_fma_f32 v[114:115], v[94:95], v[222:223], v[114:115] neg_lo:[0,0,1] neg_hi:[0,0,1]
	v_pk_fma_f32 v[116:117], v[92:93], v[220:221], v[116:117] neg_lo:[0,0,1] neg_hi:[0,0,1]
	v_cndmask_b32_e64 v91, v91, v111, s[0:1]
	v_cndmask_b32_e64 v90, v90, v110, s[0:1]
	v_cndmask_b32_e64 v89, v89, v113, s[0:1]
	v_cndmask_b32_e64 v88, v88, v112, s[0:1]
	v_mov_b32_e32 v110, v204
	v_mov_b32_e32 v111, v204
	v_lshlrev_b64 v[108:109], 11, v[188:189]
	v_cndmask_b32_e64 v95, v95, v115, s[0:1]
	v_cndmask_b32_e64 v94, v94, v114, s[0:1]
	v_cndmask_b32_e64 v93, v93, v117, s[0:1]
	v_cndmask_b32_e64 v92, v92, v116, s[0:1]
	v_pk_mul_f32 v[112:113], v[110:111], v[90:91]
	v_pk_mul_f32 v[90:91], v[204:205], v[88:89]
	v_lshl_add_u64 v[108:109], v[206:207], 0, v[108:109]
	v_pk_mul_f32 v[94:95], v[110:111], v[94:95]
	v_pk_mul_f32 v[92:93], v[204:205], v[92:93]
	v_pk_mul_f32 v[82:83], v[82:83], v[202:203] op_sel_hi:[1,0]
	v_cvt_pk_bf16_f32 v88, v92, v93
	v_cvt_pk_bf16_f32 v89, v94, v95
	v_cvt_pk_bf16_f32 v90, v90, v91
	v_cvt_pk_bf16_f32 v91, v112, v113
	v_pk_mul_f32 v[80:81], v[80:81], v[202:203] op_sel_hi:[1,0]
	global_store_dwordx4 v[108:109], v[88:91], off sc1
	v_pk_mul_f32 v[86:87], v[86:87], v[202:203] op_sel_hi:[1,0]
	v_pk_mul_f32 v[84:85], v[84:85], v[202:203] op_sel_hi:[1,0]
	v_pk_mul_f32 v[88:89], v[82:83], v[222:223]
	v_pk_mul_f32 v[90:91], v[80:81], v[220:221]
	v_pk_fma_f32 v[88:89], v[86:87], v[226:227], v[88:89]
	v_pk_fma_f32 v[90:91], v[84:85], v[224:225], v[90:91]
	v_pk_mul_f32 v[92:93], v[82:83], v[226:227]
	v_pk_mul_f32 v[94:95], v[80:81], v[224:225]
	v_pk_fma_f32 v[92:93], v[86:87], v[222:223], v[92:93] neg_lo:[0,0,1] neg_hi:[0,0,1]
	v_pk_fma_f32 v[94:95], v[84:85], v[220:221], v[94:95] neg_lo:[0,0,1] neg_hi:[0,0,1]
	v_cndmask_b32_e64 v83, v83, v89, s[0:1]
	v_cndmask_b32_e64 v82, v82, v88, s[0:1]
	v_cndmask_b32_e64 v81, v81, v91, s[0:1]
	v_cndmask_b32_e64 v80, v80, v90, s[0:1]
	v_cndmask_b32_e64 v87, v87, v93, s[0:1]
	v_cndmask_b32_e64 v86, v86, v92, s[0:1]
	v_cndmask_b32_e64 v85, v85, v95, s[0:1]
; #define EFENCE() asm volatile("" ::: "memory")
;     __device__ __forceinline__ bool operator()(f32x4 (&acc)[2][2][4][2], const pg8::Unit& u, int wr, int wc, int fr, int fq) const {
;     ...
;         if (pn < 8) {
;             bf16_t* dst = pn < 4 ? Q : Kb; const float sc = pn < 4 ? QSCALE : 1.0f; const int colb = (pn & 3) * 256 + wc * 32 + 8 * fq;
;             const bool rot = ((wc & 1) == 0) && (fq < 2);
; #pragma unroll
;             for (int ai = 0; ai < 2; ++ai)
; #pragma unroll
;               for (int mh = 0; mh < 2; ++mh) {
;                 f32x4 c4[2], s4[2];
; #pragma unroll
;                 for (int q = 0; q < 2; ++q) { c4[q] = (f32x4){1.f, 1.f, 1.f, 1.f}; s4[q] = (f32x4){0.f, 0.f, 0.f, 0.f};
;                     if (rot) { const int t = (row0 + ai * 128 + (2 * mh + q) * 16) & (SEQ - 1); c4[q] = *(const f32x4*)(cosT + t * 8 + 4 * fq); s4[q] = *(const f32x4*)(sinT + t * 8 + 4 * fq); } }
; #pragma unroll
;                 for (int q = 0; q < 2; ++q) { const int m = 2 * mh + q; const int row = row0 + ai * 128 + m * 16; const float rsv = RS_AT(ai, m);
; #pragma unroll
;                     for (int bj = 0; bj < 2; ++bj) { f32x4 x1 = acc[ai][bj][m][0] * rsv, x2 = acc[ai][bj][m][1] * rsv;
;                         const f32x4 y1 = x1 * c4[q] - x2 * s4[q], y2 = x2 * c4[q] + x1 * s4[q];
;                         if (rot) { x1 = y1; x2 = y2; }
;                         st8(dst + (size_t)row * DM + colb + bj * 128, x1 * sc, x2 * sc); } }
;                 EFENCE(); }
	v_cndmask_b32_e64 v84, v84, v94, s[0:1]
	v_pk_mul_f32 v[88:89], v[110:111], v[82:83]
	v_pk_mul_f32 v[82:83], v[204:205], v[80:81]
	v_pk_mul_f32 v[86:87], v[110:111], v[86:87]
	v_pk_mul_f32 v[84:85], v[204:205], v[84:85]
	v_pk_mul_f32 v[74:75], v[74:75], v[200:201] op_sel_hi:[1,0]
	v_cvt_pk_bf16_f32 v80, v84, v85
	v_cvt_pk_bf16_f32 v81, v86, v87
	v_cvt_pk_bf16_f32 v82, v82, v83
	v_cvt_pk_bf16_f32 v83, v88, v89
	v_pk_mul_f32 v[72:73], v[72:73], v[200:201] op_sel_hi:[1,0]
	global_store_dwordx4 v[108:109], v[80:83], off offset:256 sc1
	v_pk_mul_f32 v[78:79], v[78:79], v[200:201] op_sel_hi:[1,0]
	v_pk_mul_f32 v[76:77], v[76:77], v[200:201] op_sel_hi:[1,0]
	v_pk_mul_f32 v[82:83], v[72:73], v[228:229]
	v_pk_mul_f32 v[84:85], v[74:75], v[230:231]
	v_pk_fma_f32 v[82:83], v[76:77], v[232:233], v[82:83]
	v_pk_fma_f32 v[84:85], v[78:79], v[234:235], v[84:85]
	v_pk_mul_f32 v[86:87], v[72:73], v[232:233]
	v_pk_mul_f32 v[88:89], v[74:75], v[234:235]
	v_pk_fma_f32 v[86:87], v[76:77], v[228:229], v[86:87] neg_lo:[0,0,1] neg_hi:[0,0,1]
	v_pk_fma_f32 v[88:89], v[78:79], v[230:231], v[88:89] neg_lo:[0,0,1] neg_hi:[0,0,1]
	v_cndmask_b32_e64 v75, v75, v85, s[0:1]
	v_cndmask_b32_e64 v74, v74, v84, s[0:1]
	v_cndmask_b32_e64 v73, v73, v83, s[0:1]
	v_cndmask_b32_e64 v72, v72, v82, s[0:1]
	v_lshlrev_b64 v[80:81], 11, v[186:187]
	v_cndmask_b32_e64 v79, v79, v89, s[0:1]
	v_cndmask_b32_e64 v78, v78, v88, s[0:1]
	v_cndmask_b32_e64 v77, v77, v87, s[0:1]
	v_cndmask_b32_e64 v76, v76, v86, s[0:1]
	v_pk_mul_f32 v[82:83], v[110:111], v[74:75]
	v_pk_mul_f32 v[74:75], v[204:205], v[72:73]
	v_lshl_add_u64 v[80:81], v[206:207], 0, v[80:81]
	v_pk_mul_f32 v[78:79], v[110:111], v[78:79]
	v_pk_mul_f32 v[76:77], v[204:205], v[76:77]
	v_pk_mul_f32 v[66:67], v[66:67], v[200:201] op_sel_hi:[1,0]
	v_cvt_pk_bf16_f32 v72, v76, v77
	v_cvt_pk_bf16_f32 v73, v78, v79
	v_cvt_pk_bf16_f32 v74, v74, v75
	v_cvt_pk_bf16_f32 v75, v82, v83
	v_pk_mul_f32 v[64:65], v[64:65], v[200:201] op_sel_hi:[1,0]
	global_store_dwordx4 v[80:81], v[72:75], off sc1
	v_pk_mul_f32 v[70:71], v[70:71], v[200:201] op_sel_hi:[1,0]
	v_pk_mul_f32 v[68:69], v[68:69], v[200:201] op_sel_hi:[1,0]
	v_pk_mul_f32 v[72:73], v[64:65], v[228:229]
	v_pk_mul_f32 v[74:75], v[66:67], v[230:231]
	v_pk_fma_f32 v[72:73], v[68:69], v[232:233], v[72:73]
	v_pk_fma_f32 v[74:75], v[70:71], v[234:235], v[74:75]
	v_pk_mul_f32 v[76:77], v[64:65], v[232:233]
	v_pk_mul_f32 v[78:79], v[66:67], v[234:235]
	v_pk_fma_f32 v[76:77], v[68:69], v[228:229], v[76:77] neg_lo:[0,0,1] neg_hi:[0,0,1]
	v_pk_fma_f32 v[78:79], v[70:71], v[230:231], v[78:79] neg_lo:[0,0,1] neg_hi:[0,0,1]
	v_cndmask_b32_e64 v67, v67, v75, s[0:1]
	v_cndmask_b32_e64 v66, v66, v74, s[0:1]
	v_cndmask_b32_e64 v65, v65, v73, s[0:1]
	v_cndmask_b32_e64 v64, v64, v72, s[0:1]
	v_cndmask_b32_e64 v71, v71, v79, s[0:1]
	v_cndmask_b32_e64 v70, v70, v78, s[0:1]
	v_cndmask_b32_e64 v69, v69, v77, s[0:1]
	v_cndmask_b32_e64 v68, v68, v76, s[0:1]
	v_pk_mul_f32 v[72:73], v[110:111], v[66:67]
	v_pk_mul_f32 v[66:67], v[204:205], v[64:65]
	v_pk_mul_f32 v[70:71], v[110:111], v[70:71]
	v_pk_mul_f32 v[68:69], v[204:205], v[68:69]
	v_mov_b32_e32 v74, 0
	v_cvt_pk_bf16_f32 v64, v68, v69
	v_cvt_pk_bf16_f32 v65, v70, v71
	v_cvt_pk_bf16_f32 v66, v66, v67
	v_cvt_pk_bf16_f32 v67, v72, v73
	global_store_dwordx4 v[80:81], v[64:67], off offset:256 sc1
	v_mov_b32_e32 v68, 0
	v_mov_b32_e32 v72, 0
	v_mov_b32_e32 v65, 0x400
	v_mov_b32_e32 v64, 1.0
	v_lshl_add_u32 v80, v184, 3, v65
	v_mov_b32_e32 v73, 0
	v_mov_b32_e32 v75, 0
	v_mov_b32_e32 v76, 1.0
	v_mov_b32_e32 v77, 1.0
	v_mov_b32_e32 v78, 1.0
	v_mov_b32_e32 v79, 1.0
	s_and_saveexec_b64 s[4:5], s[0:1]
	s_cbranch_execz .LBB0_745
	v_and_b32_e32 v65, 0x3e78, v80
	v_lshlrev_b32_e32 v160, 2, v65
	v_lshl_add_u64 v[66:67], v[168:169], 0, v[160:161]
	v_lshl_add_u64 v[70:71], v[170:171], 0, v[160:161]
	global_load_dwordx4 v[76:79], v[66:67], off
	global_load_dwordx4 v[72:75], v[70:71], off

; #define EFENCE() asm volatile("" ::: "memory")
;     __device__ __forceinline__ bool operator()(f32x4 (&acc)[2][2][4][2], const pg8::Unit& u, int wr, int wc, int fr, int fq) const {
;     ...
;         if (pn < 8) {
;             bf16_t* dst = pn < 4 ? Q : Kb; const float sc = pn < 4 ? QSCALE : 1.0f; const int colb = (pn & 3) * 256 + wc * 32 + 8 * fq;
;             const bool rot = ((wc & 1) == 0) && (fq < 2);
; #pragma unroll
;             for (int ai = 0; ai < 2; ++ai)
; #pragma unroll
;               for (int mh = 0; mh < 2; ++mh) {
;                 f32x4 c4[2], s4[2];
; #pragma unroll
;                 for (int q = 0; q < 2; ++q) { c4[q] = (f32x4){1.f, 1.f, 1.f, 1.f}; s4[q] = (f32x4){0.f, 0.f, 0.f, 0.f};
;                     if (rot) { const int t = (row0 + ai * 128 + (2 * mh + q) * 16) & (SEQ - 1); c4[q] = *(const f32x4*)(cosT + t * 8 + 4 * fq); s4[q] = *(const f32x4*)(sinT + t * 8 + 4 * fq); } }
; #pragma unroll
;                 for (int q = 0; q < 2; ++q) { const int m = 2 * mh + q; const int row = row0 + ai * 128 + m * 16; const float rsv = RS_AT(ai, m);
; #pragma unroll
;                     for (int bj = 0; bj < 2; ++bj) { f32x4 x1 = acc[ai][bj][m][0] * rsv, x2 = acc[ai][bj][m][1] * rsv;
;                         const f32x4 y1 = x1 * c4[q] - x2 * s4[q], y2 = x2 * c4[q] + x1 * s4[q];
;                         if (rot) { x1 = y1; x2 = y2; }
;                         st8(dst + (size_t)row * DM + colb + bj * 128, x1 * sc, x2 * sc); } }
;                 EFENCE(); }
.Lrot_749:
	s_or_b64 exec, exec, s[4:5]
	v_pk_mul_f32 v[58:59], v[58:59], v[152:153] op_sel_hi:[1,0]
	v_pk_mul_f32 v[56:57], v[56:57], v[152:153] op_sel_hi:[1,0]
	v_pk_mul_f32 v[62:63], v[62:63], v[152:153] op_sel_hi:[1,0]
	v_pk_mul_f32 v[60:61], v[60:61], v[152:153] op_sel_hi:[1,0]
	s_waitcnt vmcnt(5)
	v_pk_mul_f32 v[84:85], v[58:59], v[78:79]
	v_pk_mul_f32 v[86:87], v[56:57], v[76:77]
	s_waitcnt vmcnt(0)
	v_pk_fma_f32 v[84:85], v[62:63], v[74:75], v[84:85]
	v_pk_fma_f32 v[86:87], v[60:61], v[72:73], v[86:87]
	v_pk_mul_f32 v[88:89], v[58:59], v[74:75]
	v_pk_mul_f32 v[90:91], v[56:57], v[72:73]
	v_pk_fma_f32 v[88:89], v[62:63], v[78:79], v[88:89] neg_lo:[0,0,1] neg_hi:[0,0,1]
	v_pk_fma_f32 v[90:91], v[60:61], v[76:77], v[90:91] neg_lo:[0,0,1] neg_hi:[0,0,1]
	v_cndmask_b32_e64 v59, v59, v85, s[0:1]
	v_cndmask_b32_e64 v58, v58, v84, s[0:1]
	v_cndmask_b32_e64 v57, v57, v87, s[0:1]
	v_cndmask_b32_e64 v56, v56, v86, s[0:1]
	v_mov_b32_e32 v84, v204
	v_mov_b32_e32 v85, v204
	v_lshlrev_b64 v[82:83], 11, v[182:183]
	v_cndmask_b32_e64 v63, v63, v89, s[0:1]
	v_cndmask_b32_e64 v62, v62, v88, s[0:1]
	v_cndmask_b32_e64 v61, v61, v91, s[0:1]
	v_cndmask_b32_e64 v60, v60, v90, s[0:1]
	v_pk_mul_f32 v[86:87], v[84:85], v[58:59]
	v_pk_mul_f32 v[58:59], v[204:205], v[56:57]
	v_lshl_add_u64 v[82:83], v[206:207], 0, v[82:83]
	v_pk_mul_f32 v[62:63], v[84:85], v[62:63]
	v_pk_mul_f32 v[60:61], v[204:205], v[60:61]
	v_pk_mul_f32 v[50:51], v[50:51], v[152:153] op_sel_hi:[1,0]
	v_cvt_pk_bf16_f32 v56, v60, v61
	v_cvt_pk_bf16_f32 v57, v62, v63
	v_cvt_pk_bf16_f32 v58, v58, v59
	v_cvt_pk_bf16_f32 v59, v86, v87
	v_pk_mul_f32 v[48:49], v[48:49], v[152:153] op_sel_hi:[1,0]
	global_store_dwordx4 v[82:83], v[56:59], off sc1
	v_pk_mul_f32 v[54:55], v[54:55], v[152:153] op_sel_hi:[1,0]
	v_pk_mul_f32 v[52:53], v[52:53], v[152:153] op_sel_hi:[1,0]
	v_pk_mul_f32 v[56:57], v[50:51], v[78:79]
	v_pk_mul_f32 v[58:59], v[48:49], v[76:77]
	v_pk_fma_f32 v[56:57], v[54:55], v[74:75], v[56:57]
	v_pk_fma_f32 v[58:59], v[52:53], v[72:73], v[58:59]
	v_pk_mul_f32 v[60:61], v[50:51], v[74:75]
	v_pk_mul_f32 v[62:63], v[48:49], v[72:73]
	v_pk_fma_f32 v[60:61], v[54:55], v[78:79], v[60:61] neg_lo:[0,0,1] neg_hi:[0,0,1]
	v_pk_fma_f32 v[62:63], v[52:53], v[76:77], v[62:63] neg_lo:[0,0,1] neg_hi:[0,0,1]
	v_cndmask_b32_e64 v51, v51, v57, s[0:1]
	v_cndmask_b32_e64 v50, v50, v56, s[0:1]
	v_cndmask_b32_e64 v49, v49, v59, s[0:1]
	v_cndmask_b32_e64 v48, v48, v58, s[0:1]
	v_cndmask_b32_e64 v55, v55, v61, s[0:1]
	v_cndmask_b32_e64 v54, v54, v60, s[0:1]
	v_cndmask_b32_e64 v53, v53, v63, s[0:1]
	v_cndmask_b32_e64 v52, v52, v62, s[0:1]
	v_pk_mul_f32 v[56:57], v[84:85], v[50:51]
	v_pk_mul_f32 v[50:51], v[204:205], v[48:49]
	v_pk_mul_f32 v[54:55], v[84:85], v[54:55]
	v_pk_mul_f32 v[52:53], v[204:205], v[52:53]
	v_pk_mul_f32 v[42:43], v[42:43], v[150:151] op_sel_hi:[1,0]
	v_cvt_pk_bf16_f32 v48, v52, v53
	v_cvt_pk_bf16_f32 v49, v54, v55
	v_cvt_pk_bf16_f32 v50, v50, v51
	v_cvt_pk_bf16_f32 v51, v56, v57
	v_pk_mul_f32 v[40:41], v[40:41], v[150:151] op_sel_hi:[1,0]
	global_store_dwordx4 v[82:83], v[48:51], off offset:256 sc1
	v_pk_mul_f32 v[46:47], v[46:47], v[150:151] op_sel_hi:[1,0]
	v_pk_mul_f32 v[44:45], v[44:45], v[150:151] op_sel_hi:[1,0]
	v_pk_mul_f32 v[50:51], v[40:41], v[64:65]
	v_pk_mul_f32 v[52:53], v[42:43], v[66:67]
	v_pk_fma_f32 v[50:51], v[44:45], v[68:69], v[50:51]
	v_pk_fma_f32 v[52:53], v[46:47], v[70:71], v[52:53]
	v_pk_mul_f32 v[54:55], v[40:41], v[68:69]
	v_pk_mul_f32 v[56:57], v[42:43], v[70:71]
	v_pk_fma_f32 v[54:55], v[44:45], v[64:65], v[54:55] neg_lo:[0,0,1] neg_hi:[0,0,1]
	v_pk_fma_f32 v[56:57], v[46:47], v[66:67], v[56:57] neg_lo:[0,0,1] neg_hi:[0,0,1]
	v_cndmask_b32_e64 v43, v43, v53, s[0:1]
	v_cndmask_b32_e64 v42, v42, v52, s[0:1]
	v_cndmask_b32_e64 v41, v41, v51, s[0:1]
	v_cndmask_b32_e64 v40, v40, v50, s[0:1]
	v_lshlrev_b64 v[48:49], 11, v[180:181]
	v_cndmask_b32_e64 v47, v47, v57, s[0:1]
	v_cndmask_b32_e64 v46, v46, v56, s[0:1]
	v_cndmask_b32_e64 v45, v45, v55, s[0:1]
	v_cndmask_b32_e64 v44, v44, v54, s[0:1]
	v_pk_mul_f32 v[50:51], v[84:85], v[42:43]
	v_pk_mul_f32 v[42:43], v[204:205], v[40:41]
	v_lshl_add_u64 v[48:49], v[206:207], 0, v[48:49]
	v_pk_mul_f32 v[46:47], v[84:85], v[46:47]
	v_pk_mul_f32 v[44:45], v[204:205], v[44:45]
	v_pk_mul_f32 v[34:35], v[34:35], v[150:151] op_sel_hi:[1,0]
	v_cvt_pk_bf16_f32 v40, v44, v45
	v_cvt_pk_bf16_f32 v41, v46, v47
	v_cvt_pk_bf16_f32 v42, v42, v43
	v_cvt_pk_bf16_f32 v43, v50, v51
	v_pk_mul_f32 v[32:33], v[32:33], v[150:151] op_sel_hi:[1,0]
	global_store_dwordx4 v[48:49], v[40:43], off sc1
	v_pk_mul_f32 v[38:39], v[38:39], v[150:151] op_sel_hi:[1,0]
	v_pk_mul_f32 v[36:37], v[36:37], v[150:151] op_sel_hi:[1,0]
	v_pk_mul_f32 v[40:41], v[32:33], v[64:65]
	v_pk_mul_f32 v[42:43], v[34:35], v[66:67]
	v_pk_fma_f32 v[40:41], v[36:37], v[68:69], v[40:41]
	v_pk_fma_f32 v[42:43], v[38:39], v[70:71], v[42:43]
	v_pk_mul_f32 v[44:45], v[32:33], v[68:69]
	v_pk_mul_f32 v[46:47], v[34:35], v[70:71]
	v_pk_fma_f32 v[44:45], v[36:37], v[64:65], v[44:45] neg_lo:[0,0,1] neg_hi:[0,0,1]
	v_pk_fma_f32 v[46:47], v[38:39], v[66:67], v[46:47] neg_lo:[0,0,1] neg_hi:[0,0,1]
	v_cndmask_b32_e64 v35, v35, v43, s[0:1]
	v_cndmask_b32_e64 v34, v34, v42, s[0:1]
	v_cndmask_b32_e64 v33, v33, v41, s[0:1]
	v_cndmask_b32_e64 v32, v32, v40, s[0:1]
	v_cndmask_b32_e64 v39, v39, v47, s[0:1]
	v_cndmask_b32_e64 v38, v38, v46, s[0:1]
	v_cndmask_b32_e64 v37, v37, v45, s[0:1]
	v_cndmask_b32_e64 v36, v36, v44, s[0:1]
	v_pk_mul_f32 v[40:41], v[84:85], v[34:35]
	v_pk_mul_f32 v[34:35], v[204:205], v[32:33]
	v_pk_mul_f32 v[38:39], v[84:85], v[38:39]
	v_pk_mul_f32 v[36:37], v[204:205], v[36:37]
; #define EFENCE() asm volatile("" ::: "memory")
;     __device__ __forceinline__ bool operator()(f32x4 (&acc)[2][2][4][2], const pg8::Unit& u, int wr, int wc, int fr, int fq) const {
;     ...
;         if (pn < 8) {
;             bf16_t* dst = pn < 4 ? Q : Kb; const float sc = pn < 4 ? QSCALE : 1.0f; const int colb = (pn & 3) * 256 + wc * 32 + 8 * fq;
;             const bool rot = ((wc & 1) == 0) && (fq < 2);
; #pragma unroll
;             for (int ai = 0; ai < 2; ++ai)
; #pragma unroll
;               for (int mh = 0; mh < 2; ++mh) {
;                 f32x4 c4[2], s4[2];
; #pragma unroll
;                 for (int q = 0; q < 2; ++q) { c4[q] = (f32x4){1.f, 1.f, 1.f, 1.f}; s4[q] = (f32x4){0.f, 0.f, 0.f, 0.f};
;                     if (rot) { const int t = (row0 + ai * 128 + (2 * mh + q) * 16) & (SEQ - 1); c4[q] = *(const f32x4*)(cosT + t * 8 + 4 * fq); s4[q] = *(const f32x4*)(sinT + t * 8 + 4 * fq); } }
; #pragma unroll
;                 for (int q = 0; q < 2; ++q) { const int m = 2 * mh + q; const int row = row0 + ai * 128 + m * 16; const float rsv = RS_AT(ai, m);
; #pragma unroll
;                     for (int bj = 0; bj < 2; ++bj) { f32x4 x1 = acc[ai][bj][m][0] * rsv, x2 = acc[ai][bj][m][1] * rsv;
;                         const f32x4 y1 = x1 * c4[q] - x2 * s4[q], y2 = x2 * c4[q] + x1 * s4[q];
;                         if (rot) { x1 = y1; x2 = y2; }
;                         st8(dst + (size_t)row * DM + colb + bj * 128, x1 * sc, x2 * sc); } }
;                 EFENCE(); }
	v_mov_b32_e32 v42, 0
	v_cvt_pk_bf16_f32 v32, v36, v37
	v_cvt_pk_bf16_f32 v33, v38, v39
	v_cvt_pk_bf16_f32 v34, v34, v35
	v_cvt_pk_bf16_f32 v35, v40, v41
	global_store_dwordx4 v[48:49], v[32:35], off offset:256 sc1
	v_pk_mul_f32 v[26:27], v[26:27], v[148:149] op_sel_hi:[1,0]
	v_pk_mul_f32 v[24:25], v[24:25], v[148:149] op_sel_hi:[1,0]
	v_pk_mul_f32 v[30:31], v[30:31], v[148:149] op_sel_hi:[1,0]
	v_pk_mul_f32 v[28:29], v[28:29], v[148:149] op_sel_hi:[1,0]
	v_pk_mul_f32 v[50:51], v[26:27], v[222:223]
	v_pk_mul_f32 v[52:53], v[24:25], v[220:221]
	v_pk_fma_f32 v[50:51], v[30:31], v[226:227], v[50:51]
	v_pk_fma_f32 v[52:53], v[28:29], v[224:225], v[52:53]
	v_pk_mul_f32 v[54:55], v[26:27], v[226:227]
	v_pk_mul_f32 v[56:57], v[24:25], v[224:225]
	v_pk_fma_f32 v[54:55], v[30:31], v[222:223], v[54:55] neg_lo:[0,0,1] neg_hi:[0,0,1]
	v_pk_fma_f32 v[56:57], v[28:29], v[220:221], v[56:57] neg_lo:[0,0,1] neg_hi:[0,0,1]
	v_cndmask_b32_e64 v27, v27, v51, s[0:1]
	v_cndmask_b32_e64 v26, v26, v50, s[0:1]
	v_cndmask_b32_e64 v25, v25, v53, s[0:1]
	v_cndmask_b32_e64 v24, v24, v52, s[0:1]
	v_mov_b32_e32 v50, v204
	v_mov_b32_e32 v51, v204
	v_lshlrev_b64 v[48:49], 11, v[178:179]
	v_cndmask_b32_e64 v31, v31, v55, s[0:1]
	v_cndmask_b32_e64 v30, v30, v54, s[0:1]
	v_cndmask_b32_e64 v29, v29, v57, s[0:1]
	v_cndmask_b32_e64 v28, v28, v56, s[0:1]
	v_pk_mul_f32 v[52:53], v[50:51], v[26:27]
	v_pk_mul_f32 v[26:27], v[204:205], v[24:25]
	v_lshl_add_u64 v[48:49], v[206:207], 0, v[48:49]
	v_pk_mul_f32 v[30:31], v[50:51], v[30:31]
	v_pk_mul_f32 v[28:29], v[204:205], v[28:29]
	v_pk_mul_f32 v[18:19], v[18:19], v[148:149] op_sel_hi:[1,0]
	v_cvt_pk_bf16_f32 v24, v28, v29
	v_cvt_pk_bf16_f32 v25, v30, v31
	v_cvt_pk_bf16_f32 v26, v26, v27
	v_cvt_pk_bf16_f32 v27, v52, v53
	v_pk_mul_f32 v[16:17], v[16:17], v[148:149] op_sel_hi:[1,0]
	global_store_dwordx4 v[48:49], v[24:27], off sc1
	v_pk_mul_f32 v[22:23], v[22:23], v[148:149] op_sel_hi:[1,0]
	v_pk_mul_f32 v[20:21], v[20:21], v[148:149] op_sel_hi:[1,0]
	v_pk_mul_f32 v[24:25], v[18:19], v[222:223]
	v_pk_mul_f32 v[26:27], v[16:17], v[220:221]
	v_pk_fma_f32 v[24:25], v[22:23], v[226:227], v[24:25]
	v_pk_fma_f32 v[26:27], v[20:21], v[224:225], v[26:27]
	v_pk_mul_f32 v[28:29], v[18:19], v[226:227]
	v_pk_mul_f32 v[30:31], v[16:17], v[224:225]
	v_pk_fma_f32 v[28:29], v[22:23], v[222:223], v[28:29] neg_lo:[0,0,1] neg_hi:[0,0,1]
	v_pk_fma_f32 v[30:31], v[20:21], v[220:221], v[30:31] neg_lo:[0,0,1] neg_hi:[0,0,1]
	v_cndmask_b32_e64 v19, v19, v25, s[0:1]
	v_cndmask_b32_e64 v18, v18, v24, s[0:1]
	v_cndmask_b32_e64 v17, v17, v27, s[0:1]
	v_cndmask_b32_e64 v16, v16, v26, s[0:1]
	v_cndmask_b32_e64 v23, v23, v29, s[0:1]
	v_cndmask_b32_e64 v22, v22, v28, s[0:1]
	v_cndmask_b32_e64 v21, v21, v31, s[0:1]
	v_cndmask_b32_e64 v20, v20, v30, s[0:1]
	v_pk_mul_f32 v[24:25], v[50:51], v[18:19]
	v_pk_mul_f32 v[18:19], v[204:205], v[16:17]
	v_pk_mul_f32 v[22:23], v[50:51], v[22:23]
	v_pk_mul_f32 v[20:21], v[204:205], v[20:21]
	v_pk_mul_f32 v[10:11], v[10:11], v[146:147] op_sel_hi:[1,0]
	v_cvt_pk_bf16_f32 v16, v20, v21
	v_cvt_pk_bf16_f32 v17, v22, v23
	v_cvt_pk_bf16_f32 v18, v18, v19
	v_cvt_pk_bf16_f32 v19, v24, v25
	v_pk_mul_f32 v[8:9], v[8:9], v[146:147] op_sel_hi:[1,0]
	global_store_dwordx4 v[48:49], v[16:19], off offset:256 sc1
	v_pk_mul_f32 v[14:15], v[14:15], v[146:147] op_sel_hi:[1,0]
	v_pk_mul_f32 v[12:13], v[12:13], v[146:147] op_sel_hi:[1,0]
	v_pk_mul_f32 v[18:19], v[8:9], v[228:229]
	v_pk_mul_f32 v[20:21], v[10:11], v[230:231]
	v_pk_fma_f32 v[18:19], v[12:13], v[232:233], v[18:19]
	v_pk_fma_f32 v[20:21], v[14:15], v[234:235], v[20:21]
	v_pk_mul_f32 v[22:23], v[8:9], v[232:233]
	v_pk_mul_f32 v[24:25], v[10:11], v[234:235]
	v_pk_fma_f32 v[22:23], v[12:13], v[228:229], v[22:23] neg_lo:[0,0,1] neg_hi:[0,0,1]
	v_pk_fma_f32 v[24:25], v[14:15], v[230:231], v[24:25] neg_lo:[0,0,1] neg_hi:[0,0,1]
	v_cndmask_b32_e64 v11, v11, v21, s[0:1]
	v_cndmask_b32_e64 v10, v10, v20, s[0:1]
	v_cndmask_b32_e64 v9, v9, v19, s[0:1]
	v_cndmask_b32_e64 v8, v8, v18, s[0:1]
	v_lshlrev_b64 v[16:17], 11, v[176:177]
	v_cndmask_b32_e64 v15, v15, v25, s[0:1]
	v_cndmask_b32_e64 v14, v14, v24, s[0:1]
	v_cndmask_b32_e64 v13, v13, v23, s[0:1]
	v_cndmask_b32_e64 v12, v12, v22, s[0:1]
	v_pk_mul_f32 v[18:19], v[50:51], v[10:11]
	v_pk_mul_f32 v[10:11], v[204:205], v[8:9]
	v_lshl_add_u64 v[16:17], v[206:207], 0, v[16:17]
	v_pk_mul_f32 v[14:15], v[50:51], v[14:15]
	v_pk_mul_f32 v[12:13], v[204:205], v[12:13]
	v_pk_mul_f32 v[2:3], v[2:3], v[146:147] op_sel_hi:[1,0]
	v_cvt_pk_bf16_f32 v8, v12, v13
	v_cvt_pk_bf16_f32 v9, v14, v15
	v_cvt_pk_bf16_f32 v10, v10, v11
	v_cvt_pk_bf16_f32 v11, v18, v19
	v_pk_mul_f32 v[0:1], v[0:1], v[146:147] op_sel_hi:[1,0]
	global_store_dwordx4 v[16:17], v[8:11], off sc1
	v_pk_mul_f32 v[6:7], v[6:7], v[146:147] op_sel_hi:[1,0]
	v_pk_mul_f32 v[4:5], v[4:5], v[146:147] op_sel_hi:[1,0]
	v_pk_mul_f32 v[8:9], v[0:1], v[228:229]
	v_pk_mul_f32 v[10:11], v[2:3], v[230:231]
	v_pk_fma_f32 v[8:9], v[4:5], v[232:233], v[8:9]
	v_pk_fma_f32 v[10:11], v[6:7], v[234:235], v[10:11]
	v_pk_mul_f32 v[12:13], v[0:1], v[232:233]
	v_pk_mul_f32 v[14:15], v[2:3], v[234:235]
	v_pk_fma_f32 v[12:13], v[4:5], v[228:229], v[12:13] neg_lo:[0,0,1] neg_hi:[0,0,1]
	v_pk_fma_f32 v[14:15], v[6:7], v[230:231], v[14:15] neg_lo:[0,0,1] neg_hi:[0,0,1]
	v_cndmask_b32_e64 v3, v3, v11, s[0:1]
	v_cndmask_b32_e64 v2, v2, v10, s[0:1]
	v_cndmask_b32_e64 v1, v1, v9, s[0:1]
	v_cndmask_b32_e64 v0, v0, v8, s[0:1]
	v_cndmask_b32_e64 v7, v7, v15, s[0:1]
	v_cndmask_b32_e64 v6, v6, v14, s[0:1]
	v_cndmask_b32_e64 v5, v5, v13, s[0:1]
	v_cndmask_b32_e64 v4, v4, v12, s[0:1]
	v_pk_mul_f32 v[8:9], v[50:51], v[2:3]
	v_pk_mul_f32 v[2:3], v[204:205], v[0:1]
	v_pk_mul_f32 v[6:7], v[50:51], v[6:7]
	v_pk_mul_f32 v[4:5], v[204:205], v[4:5]
	s_nop 0
	v_cvt_pk_bf16_f32 v0, v4, v5
	v_cvt_pk_bf16_f32 v1, v6, v7
	v_cvt_pk_bf16_f32 v2, v2, v3
	v_cvt_pk_bf16_f32 v3, v8, v9
	global_store_dwordx4 v[16:17], v[0:3], off offset:256 sc1
	s_andn2_b64 vcc, exec, s[6:7]
	s_mov_b64 s[4:5], -1
	s_cbranch_vccnz .LBB0_712

; __device__ __forceinline__ float bf_lo(unsigned w) { return __uint_as_float(w << 16); }
; __device__ __forceinline__ float bf_hi(unsigned w) { return __uint_as_float(w & 0xffff0000u); }
; __device__ __forceinline__ float wave_sum(float v) { return half_sum(sum32(v)); }
; __device__ __forceinline__ void st_bf4(bf16_t* p, f32x4 v) { u32x2 w; w.x = cvt_pk_bf16(v[0], v[1]); w.y = cvt_pk_bf16(v[2], v[3]); *(u32x2*)p = w; }
; template <int NTK>
; __device__ __forceinline__ void combine_rows(int t0, int tstride, const LAS int* bst, const int* tok_e, const int* tok_pos, const float* tok_w, const bf16_t* Y, const bf16_t* xbi, float* xio, bf16_t* xb, float* part, const float* gfin, bool last, int lane) {
;     ...
;     for (int i = 0; i < NTK; ++i) { float s = 0.f;
; #pragma unroll
;         for (int j = 0; j < 4; ++j) { const f32x4 a = {bf_lo(ya[i][j].x), bf_hi(ya[i][j].x), bf_lo(ya[i][j].y), bf_hi(ya[i][j].y)}, b = {bf_lo(yb[i][j].x), bf_hi(yb[i][j].x), bf_lo(yb[i][j].y), bf_hi(yb[i][j].y)};
;             v[i][j] = v[i][j] + w0[i] * a + w1[i] * b;
;             s += (v[i][j][0] * v[i][j][0] + v[i][j][1] * v[i][j][1]) + (v[i][j][2] * v[i][j][2] + v[i][j][3] * v[i][j][3]); }
;         s = wave_sum(s);
;         if (ok[i]) { const int t = tk[i];
;             if (!last) {
; #pragma unroll
;                 for (int j = 0; j < 4; ++j) { const int c = j * 256 + lane * 4; st_bf4(xb + (size_t)t * DM + c, v[i][j]); }
;                 if (lane < 16) part[(size_t)t * 16 + lane] = lane == 0 ? s : 0.f;
;             } else {
;                 const float r = 1.0f / sqrtf(s * (1.0f / DM) + EPS);
; #pragma unroll
;                 for (int j = 0; j < 4; ++j) { const int c = j * 256 + lane * 4; *(f32x4*)(xio + (size_t)t * DM + c) = v[i][j] * r * *(const f32x4*)(gfin + c); }
;             } } }
.LBB0_1637:
	s_andn2_b64 vcc, exec, s[10:11]
	s_cbranch_vccnz .LBB0_1639
	s_nop 1
	v_mov_b64_e32 v[116:117], v[216:217]
	v_mov_b64_e32 v[118:119], v[218:219]
	v_fmamk_f32 v102, v112, 0x3a800000, v212
	s_mov_b32 s2, 0xf800000
	v_cmp_gt_f32_e32 vcc, s2, v102
	v_mul_f32_e32 v103, 0x4f800000, v102
	s_nop 0
	v_cndmask_b32_e32 v102, v102, v103, vcc
	v_sqrt_f32_e32 v103, v102
	s_nop 0
	v_add_u32_e32 v112, -1, v103
	v_fma_f32 v113, -v112, v103, v102
	v_cmp_ge_f32_e64 s[10:11], 0, v113
	v_add_u32_e32 v113, 1, v103
	s_nop 0
	v_cndmask_b32_e64 v112, v103, v112, s[10:11]
	v_fma_f32 v103, -v113, v103, v102
	v_cmp_lt_f32_e64 s[10:11], 0, v103
	s_nop 1
	v_cndmask_b32_e64 v103, v112, v113, s[10:11]
	v_mul_f32_e32 v112, 0x37800000, v103
	v_cndmask_b32_e32 v103, v103, v112, vcc
	v_cmp_class_f32_e32 vcc, v102, v248
	s_nop 1
	v_cndmask_b32_e32 v102, v103, v102, vcc
	v_div_scale_f32 v103, s[2:3], v102, v102, 1.0
	v_rcp_f32_e32 v112, v103
	s_nop 0
	v_fma_f32 v113, -v103, v112, 1.0
	v_fmac_f32_e32 v112, v113, v112
	v_div_scale_f32 v113, vcc, 1.0, v102, 1.0
	v_mul_f32_e32 v114, v113, v112
	v_fma_f32 v115, -v103, v114, v113
	v_fmac_f32_e32 v114, v115, v112
	v_fma_f32 v103, -v103, v114, v113
	v_div_fmas_f32 v103, v103, v112, v114
	v_div_fixup_f32 v102, v103, v102, 1.0
	v_pk_mul_f32 v[112:113], v[138:139], v[102:103] op_sel_hi:[1,0]
	v_pk_mul_f32 v[114:115], v[136:137], v[102:103] op_sel_hi:[1,0]
	v_pk_mul_f32 v[104:105], v[104:105], v[102:103] op_sel_hi:[1,0]
	v_pk_mul_f32 v[108:109], v[108:109], v[102:103] op_sel_hi:[1,0]
	v_pk_mul_f32 v[110:111], v[110:111], v[102:103] op_sel_hi:[1,0]
	v_pk_mul_f32 v[114:115], v[114:115], v[118:119]
	v_pk_mul_f32 v[112:113], v[112:113], v[116:117]
	global_store_dwordx4 v[10:11], v[112:115], off offset:-3072 sc1
	s_nop 1
	v_mov_b64_e32 v[112:113], v[220:221]
	v_mov_b64_e32 v[114:115], v[222:223]
	v_pk_mul_f32 v[112:113], v[108:109], v[112:113]
	v_pk_mul_f32 v[114:115], v[104:105], v[114:115]
	global_store_dwordx4 v[10:11], v[112:115], off offset:-2048 sc1
	v_pk_mul_f32 v[108:109], v[106:107], v[102:103] op_sel_hi:[1,0]
	s_nop 1
	v_mov_b64_e32 v[104:105], v[224:225]
	v_mov_b64_e32 v[106:107], v[226:227]
	v_pk_mul_f32 v[104:105], v[110:111], v[104:105]
	v_pk_mul_f32 v[106:107], v[108:109], v[106:107]
	global_store_dwordx4 v[10:11], v[104:107], off offset:-1024 sc1
	s_nop 1
	v_pk_mul_f32 v[104:105], v[82:83], v[102:103] op_sel_hi:[1,0]
	v_pk_mul_f32 v[102:103], v[84:85], v[102:103] op_sel_hi:[1,0]
	s_nop 1
	v_mov_b64_e32 v[82:83], v[228:229]
	v_mov_b64_e32 v[84:85], v[230:231]
	v_pk_mul_f32 v[82:83], v[102:103], v[82:83]
	v_pk_mul_f32 v[84:85], v[104:105], v[84:85]
	global_store_dwordx4 v[10:11], v[82:85], off sc1

; __device__ __forceinline__ float bf_lo(unsigned w) { return __uint_as_float(w << 16); }
; __device__ __forceinline__ float bf_hi(unsigned w) { return __uint_as_float(w & 0xffff0000u); }
; __device__ __forceinline__ float wave_sum(float v) { return half_sum(sum32(v)); }
; __device__ __forceinline__ void st_bf4(bf16_t* p, f32x4 v) { u32x2 w; w.x = cvt_pk_bf16(v[0], v[1]); w.y = cvt_pk_bf16(v[2], v[3]); *(u32x2*)p = w; }
; template <int NTK>
; __device__ __forceinline__ void combine_rows(int t0, int tstride, const LAS int* bst, const int* tok_e, const int* tok_pos, const float* tok_w, const bf16_t* Y, const bf16_t* xbi, float* xio, bf16_t* xb, float* part, const float* gfin, bool last, int lane) {
;     ...
;     for (int i = 0; i < NTK; ++i) { float s = 0.f;
; #pragma unroll
;         for (int j = 0; j < 4; ++j) { const f32x4 a = {bf_lo(ya[i][j].x), bf_hi(ya[i][j].x), bf_lo(ya[i][j].y), bf_hi(ya[i][j].y)}, b = {bf_lo(yb[i][j].x), bf_hi(yb[i][j].x), bf_lo(yb[i][j].y), bf_hi(yb[i][j].y)};
;             v[i][j] = v[i][j] + w0[i] * a + w1[i] * b;
;             s += (v[i][j][0] * v[i][j][0] + v[i][j][1] * v[i][j][1]) + (v[i][j][2] * v[i][j][2] + v[i][j][3] * v[i][j][3]); }
;         s = wave_sum(s);
;         if (ok[i]) { const int t = tk[i];
;             if (!last) {
; #pragma unroll
;                 for (int j = 0; j < 4; ++j) { const int c = j * 256 + lane * 4; st_bf4(xb + (size_t)t * DM + c, v[i][j]); }
;                 if (lane < 16) part[(size_t)t * 16 + lane] = lane == 0 ? s : 0.f;
;             } else {
;                 const float r = 1.0f / sqrtf(s * (1.0f / DM) + EPS);
; #pragma unroll
;                 for (int j = 0; j < 4; ++j) { const int c = j * 256 + lane * 4; *(f32x4*)(xio + (size_t)t * DM + c) = v[i][j] * r * *(const f32x4*)(gfin + c); }
;             } } }
.LBB0_1644:
	s_andn2_b64 vcc, exec, s[10:11]
	s_cbranch_vccnz .LBB0_1646
	v_fmamk_f32 v72, v76, 0x3a800000, v212
	s_mov_b32 s2, 0xf800000
	v_cmp_gt_f32_e32 vcc, s2, v72
	v_mul_f32_e32 v73, 0x4f800000, v72
	s_nop 0
	v_cndmask_b32_e32 v72, v72, v73, vcc
	v_sqrt_f32_e32 v73, v72
	s_nop 0
	v_add_u32_e32 v76, -1, v73
	v_fma_f32 v77, -v76, v73, v72
	v_cmp_ge_f32_e64 s[10:11], 0, v77
	v_add_u32_e32 v77, 1, v73
	s_nop 0
	v_cndmask_b32_e64 v76, v73, v76, s[10:11]
	v_fma_f32 v73, -v77, v73, v72
	v_cmp_lt_f32_e64 s[10:11], 0, v73
	s_nop 1
	v_cndmask_b32_e64 v73, v76, v77, s[10:11]
	v_mul_f32_e32 v76, 0x37800000, v73
	v_cndmask_b32_e32 v73, v73, v76, vcc
	v_cmp_class_f32_e32 vcc, v72, v248
	s_lshl_b64 s[10:11], s[26:27], 12
	s_nop 0
	v_cndmask_b32_e32 v72, v73, v72, vcc
	v_div_scale_f32 v73, s[2:3], v72, v72, 1.0
	v_rcp_f32_e32 v76, v73
	s_nop 0
	v_fma_f32 v77, -v73, v76, 1.0
	v_fmac_f32_e32 v76, v77, v76
	v_div_scale_f32 v77, vcc, 1.0, v72, 1.0
	v_mul_f32_e32 v86, v77, v76
	v_fma_f32 v87, -v73, v86, v77
	v_fmac_f32_e32 v86, v87, v76
	v_fma_f32 v73, -v73, v86, v77
	v_div_fmas_f32 v73, v73, v76, v86
	s_nop 1
	v_mov_b64_e32 v[86:87], v[216:217]
	v_mov_b64_e32 v[88:89], v[218:219]
	v_div_fixup_f32 v72, v73, v72, 1.0
	v_pk_mul_f32 v[76:77], v[92:93], v[72:73] op_sel_hi:[1,0]
	v_pk_mul_f32 v[90:91], v[90:91], v[72:73] op_sel_hi:[1,0]
	v_pk_mul_f32 v[80:81], v[80:81], v[72:73] op_sel_hi:[1,0]
	v_pk_mul_f32 v[64:65], v[64:65], v[72:73] op_sel_hi:[1,0]
	v_pk_mul_f32 v[88:89], v[90:91], v[88:89]
	v_pk_mul_f32 v[86:87], v[76:77], v[86:87]
	v_lshl_add_u64 v[90:91], v[6:7], 0, s[10:11]
	global_store_dwordx4 v[90:91], v[86:89], off sc1
	v_pk_mul_f32 v[76:77], v[82:83], v[72:73] op_sel_hi:[1,0]
	s_nop 0
	v_pk_mul_f32 v[86:87], v[84:85], v[72:73] op_sel_hi:[1,0]
	s_nop 1
	v_mov_b64_e32 v[82:83], v[220:221]
	v_mov_b64_e32 v[84:85], v[222:223]
	v_pk_mul_f32 v[82:83], v[86:87], v[82:83]
	v_pk_mul_f32 v[84:85], v[76:77], v[84:85]
	global_store_dwordx4 v[90:91], v[82:85], off offset:1024 sc1
	s_nop 1
	v_pk_mul_f32 v[82:83], v[78:79], v[72:73] op_sel_hi:[1,0]
	s_nop 1
	v_mov_b64_e32 v[76:77], v[224:225]
	v_mov_b64_e32 v[78:79], v[226:227]
	v_pk_mul_f32 v[76:77], v[80:81], v[76:77]
	v_pk_mul_f32 v[78:79], v[82:83], v[78:79]
	global_store_dwordx4 v[90:91], v[76:79], off offset:2048 sc1
	s_nop 1
	v_pk_mul_f32 v[76:77], v[74:75], v[72:73] op_sel_hi:[1,0]
	s_nop 1
	v_mov_b64_e32 v[72:73], v[228:229]
	v_mov_b64_e32 v[74:75], v[230:231]
	v_pk_mul_f32 v[72:73], v[64:65], v[72:73]
	v_pk_mul_f32 v[74:75], v[76:77], v[74:75]
	global_store_dwordx4 v[90:91], v[72:75], off offset:3072 sc1

; __device__ __forceinline__ float bf_lo(unsigned w) { return __uint_as_float(w << 16); }
; __device__ __forceinline__ float bf_hi(unsigned w) { return __uint_as_float(w & 0xffff0000u); }
; __device__ __forceinline__ float wave_sum(float v) { return half_sum(sum32(v)); }
; __device__ __forceinline__ void st_bf4(bf16_t* p, f32x4 v) { u32x2 w; w.x = cvt_pk_bf16(v[0], v[1]); w.y = cvt_pk_bf16(v[2], v[3]); *(u32x2*)p = w; }
; template <int NTK>
; __device__ __forceinline__ void combine_rows(int t0, int tstride, const LAS int* bst, const int* tok_e, const int* tok_pos, const float* tok_w, const bf16_t* Y, const bf16_t* xbi, float* xio, bf16_t* xb, float* part, const float* gfin, bool last, int lane) {
;     ...
;     for (int i = 0; i < NTK; ++i) { float s = 0.f;
; #pragma unroll
;         for (int j = 0; j < 4; ++j) { const f32x4 a = {bf_lo(ya[i][j].x), bf_hi(ya[i][j].x), bf_lo(ya[i][j].y), bf_hi(ya[i][j].y)}, b = {bf_lo(yb[i][j].x), bf_hi(yb[i][j].x), bf_lo(yb[i][j].y), bf_hi(yb[i][j].y)};
;             v[i][j] = v[i][j] + w0[i] * a + w1[i] * b;
;             s += (v[i][j][0] * v[i][j][0] + v[i][j][1] * v[i][j][1]) + (v[i][j][2] * v[i][j][2] + v[i][j][3] * v[i][j][3]); }
;         s = wave_sum(s);
;         if (ok[i]) { const int t = tk[i];
;             if (!last) {
; #pragma unroll
;                 for (int j = 0; j < 4; ++j) { const int c = j * 256 + lane * 4; st_bf4(xb + (size_t)t * DM + c, v[i][j]); }
;                 if (lane < 16) part[(size_t)t * 16 + lane] = lane == 0 ? s : 0.f;
;             } else {
;                 const float r = 1.0f / sqrtf(s * (1.0f / DM) + EPS);
; #pragma unroll
;                 for (int j = 0; j < 4; ++j) { const int c = j * 256 + lane * 4; *(f32x4*)(xio + (size_t)t * DM + c) = v[i][j] * r * *(const f32x4*)(gfin + c); }
;             } } }
.LBB0_1651:
	s_andn2_b64 vcc, exec, s[10:11]
	s_cbranch_vccnz .LBB0_1653
	v_fmamk_f32 v20, v38, 0x3a800000, v212
	s_mov_b32 s2, 0xf800000
	v_cmp_gt_f32_e32 vcc, s2, v20
	v_mul_f32_e32 v21, 0x4f800000, v20
	s_nop 0
	v_cndmask_b32_e32 v20, v20, v21, vcc
	v_sqrt_f32_e32 v21, v20
	s_nop 0
	v_add_u32_e32 v38, -1, v21
	v_fma_f32 v39, -v38, v21, v20
	v_cmp_ge_f32_e64 s[10:11], 0, v39
	v_add_u32_e32 v39, 1, v21
	s_nop 0
	v_cndmask_b32_e64 v38, v21, v38, s[10:11]
	v_fma_f32 v21, -v39, v21, v20
	v_cmp_lt_f32_e64 s[10:11], 0, v21
	s_nop 1
	v_cndmask_b32_e64 v21, v38, v39, s[10:11]
	v_mul_f32_e32 v38, 0x37800000, v21
	v_cndmask_b32_e32 v21, v21, v38, vcc
	v_cmp_class_f32_e32 vcc, v20, v248
	s_lshl_b64 s[10:11], s[22:23], 12
	s_nop 0
	v_cndmask_b32_e32 v20, v21, v20, vcc
	v_div_scale_f32 v21, s[2:3], v20, v20, 1.0
	v_rcp_f32_e32 v38, v21
	s_nop 0
	v_fma_f32 v39, -v21, v38, 1.0
	v_fmac_f32_e32 v38, v39, v38
	v_div_scale_f32 v39, vcc, 1.0, v20, 1.0
	v_mul_f32_e32 v56, v39, v38
	v_fma_f32 v57, -v21, v56, v39
	v_fmac_f32_e32 v56, v57, v38
	v_fma_f32 v21, -v21, v56, v39
	v_div_fmas_f32 v21, v21, v38, v56
	v_div_fixup_f32 v20, v21, v20, 1.0
	v_pk_mul_f32 v[38:39], v[54:55], v[20:21] op_sel_hi:[1,0]
	v_pk_mul_f32 v[56:57], v[52:53], v[20:21] op_sel_hi:[1,0]
	s_nop 1
	v_mov_b64_e32 v[52:53], v[216:217]
	v_mov_b64_e32 v[54:55], v[218:219]
	v_pk_mul_f32 v[16:17], v[16:17], v[20:21] op_sel_hi:[1,0]
	v_pk_mul_f32 v[54:55], v[56:57], v[54:55]
	v_pk_mul_f32 v[52:53], v[38:39], v[52:53]
	v_lshl_add_u64 v[56:57], v[6:7], 0, s[10:11]
	global_store_dwordx4 v[56:57], v[52:55], off sc1
	v_pk_mul_f32 v[38:39], v[48:49], v[20:21] op_sel_hi:[1,0]
	s_nop 0
	v_pk_mul_f32 v[52:53], v[50:51], v[20:21] op_sel_hi:[1,0]
	s_nop 1
	v_mov_b64_e32 v[48:49], v[220:221]
	v_mov_b64_e32 v[50:51], v[222:223]
	v_pk_mul_f32 v[48:49], v[52:53], v[48:49]
	v_pk_mul_f32 v[50:51], v[38:39], v[50:51]
	global_store_dwordx4 v[56:57], v[48:51], off offset:1024 sc1
	v_pk_mul_f32 v[38:39], v[44:45], v[20:21] op_sel_hi:[1,0]
	s_nop 0
	v_pk_mul_f32 v[48:49], v[46:47], v[20:21] op_sel_hi:[1,0]
	s_nop 1
	v_mov_b64_e32 v[44:45], v[224:225]
	v_mov_b64_e32 v[46:47], v[226:227]
	v_pk_mul_f32 v[44:45], v[48:49], v[44:45]
	v_pk_mul_f32 v[46:47], v[38:39], v[46:47]
	global_store_dwordx4 v[56:57], v[44:47], off offset:2048 sc1
	s_nop 1
	v_pk_mul_f32 v[44:45], v[36:37], v[20:21] op_sel_hi:[1,0]
	s_nop 1
	v_mov_b64_e32 v[36:37], v[228:229]
	v_mov_b64_e32 v[38:39], v[230:231]
	v_pk_mul_f32 v[36:37], v[16:17], v[36:37]
	v_pk_mul_f32 v[38:39], v[44:45], v[38:39]
	global_store_dwordx4 v[56:57], v[36:39], off offset:3072 sc1

; __device__ __forceinline__ float bf_lo(unsigned w) { return __uint_as_float(w << 16); }
; __device__ __forceinline__ float bf_hi(unsigned w) { return __uint_as_float(w & 0xffff0000u); }
; __device__ __forceinline__ float wave_sum(float v) { return half_sum(sum32(v)); }
; __device__ __forceinline__ void st_bf4(bf16_t* p, f32x4 v) { u32x2 w; w.x = cvt_pk_bf16(v[0], v[1]); w.y = cvt_pk_bf16(v[2], v[3]); *(u32x2*)p = w; }
; template <int NTK>
; __device__ __forceinline__ void combine_rows(int t0, int tstride, const LAS int* bst, const int* tok_e, const int* tok_pos, const float* tok_w, const bf16_t* Y, const bf16_t* xbi, float* xio, bf16_t* xb, float* part, const float* gfin, bool last, int lane) {
;     ...
;     for (int i = 0; i < NTK; ++i) { float s = 0.f;
; #pragma unroll
;         for (int j = 0; j < 4; ++j) { const f32x4 a = {bf_lo(ya[i][j].x), bf_hi(ya[i][j].x), bf_lo(ya[i][j].y), bf_hi(ya[i][j].y)}, b = {bf_lo(yb[i][j].x), bf_hi(yb[i][j].x), bf_lo(yb[i][j].y), bf_hi(yb[i][j].y)};
;             v[i][j] = v[i][j] + w0[i] * a + w1[i] * b;
;             s += (v[i][j][0] * v[i][j][0] + v[i][j][1] * v[i][j][1]) + (v[i][j][2] * v[i][j][2] + v[i][j][3] * v[i][j][3]); }
;         s = wave_sum(s);
;         if (ok[i]) { const int t = tk[i];
;             if (!last) {
; #pragma unroll
;                 for (int j = 0; j < 4; ++j) { const int c = j * 256 + lane * 4; st_bf4(xb + (size_t)t * DM + c, v[i][j]); }
;                 if (lane < 16) part[(size_t)t * 16 + lane] = lane == 0 ? s : 0.f;
;             } else {
;                 const float r = 1.0f / sqrtf(s * (1.0f / DM) + EPS);
; #pragma unroll
;                 for (int j = 0; j < 4; ++j) { const int c = j * 256 + lane * 4; *(f32x4*)(xio + (size_t)t * DM + c) = v[i][j] * r * *(const f32x4*)(gfin + c); }
;             } } }
.LBB0_1658:
	s_andn2_b64 vcc, exec, s[6:7]
	s_cbranch_vccnz .LBB0_1632
	v_fmamk_f32 v18, v28, 0x3a800000, v212
	s_mov_b32 s2, 0xf800000
	v_cmp_gt_f32_e32 vcc, s2, v18
	v_mul_f32_e32 v19, 0x4f800000, v18
	s_nop 0
	v_cndmask_b32_e32 v18, v18, v19, vcc
	v_sqrt_f32_e32 v19, v18
	s_nop 0
	v_add_u32_e32 v28, -1, v19
	v_fma_f32 v29, -v28, v19, v18
	v_cmp_ge_f32_e64 s[6:7], 0, v29
	v_add_u32_e32 v29, 1, v19
	s_nop 0
	v_cndmask_b32_e64 v28, v19, v28, s[6:7]
	v_fma_f32 v19, -v29, v19, v18
	v_cmp_lt_f32_e64 s[6:7], 0, v19
	s_nop 1
	v_cndmask_b32_e64 v19, v28, v29, s[6:7]
	v_mul_f32_e32 v28, 0x37800000, v19
	v_cndmask_b32_e32 v19, v19, v28, vcc
	v_cmp_class_f32_e32 vcc, v18, v248
	s_lshl_b64 s[6:7], s[18:19], 12
	s_nop 0
	v_cndmask_b32_e32 v18, v19, v18, vcc
	v_div_scale_f32 v19, s[2:3], v18, v18, 1.0
	v_rcp_f32_e32 v28, v19
	s_nop 0
	v_fma_f32 v29, -v19, v28, 1.0
	v_fmac_f32_e32 v28, v29, v28
	v_div_scale_f32 v29, vcc, 1.0, v18, 1.0
	v_mul_f32_e32 v34, v29, v28
	v_fma_f32 v35, -v19, v34, v29
	v_fmac_f32_e32 v34, v35, v28
	v_fma_f32 v19, -v19, v34, v29
	v_div_fmas_f32 v19, v19, v28, v34
	v_div_fixup_f32 v18, v19, v18, 1.0
	v_pk_mul_f32 v[34:35], v[30:31], v[18:19] op_sel_hi:[1,0]
	s_nop 1
	v_mov_b64_e32 v[28:29], v[216:217]
	v_mov_b64_e32 v[30:31], v[218:219]
	v_pk_mul_f32 v[32:33], v[32:33], v[18:19] op_sel_hi:[1,0]
	v_pk_mul_f32 v[16:17], v[16:17], v[18:19] op_sel_hi:[1,0]
	v_pk_mul_f32 v[30:31], v[34:35], v[30:31]
	v_pk_mul_f32 v[28:29], v[32:33], v[28:29]
	v_lshl_add_u64 v[32:33], v[6:7], 0, s[6:7]
	global_store_dwordx4 v[32:33], v[28:31], off sc1
	s_nop 1
	v_pk_mul_f32 v[30:31], v[26:27], v[18:19] op_sel_hi:[1,0]
	s_nop 1
	v_mov_b64_e32 v[26:27], v[220:221]
	v_mov_b64_e32 v[28:29], v[222:223]
	v_pk_mul_f32 v[26:27], v[30:31], v[26:27]
	v_pk_mul_f32 v[28:29], v[16:17], v[28:29]
	global_store_dwordx4 v[32:33], v[26:29], off offset:1024 sc1
	v_pk_mul_f32 v[16:17], v[20:21], v[18:19] op_sel_hi:[1,0]
	v_pk_mul_f32 v[20:21], v[24:25], v[18:19] op_sel_hi:[1,0]
	s_nop 1
	v_mov_b64_e32 v[24:25], v[224:225]
	v_mov_b64_e32 v[26:27], v[226:227]
	v_pk_mul_f32 v[24:25], v[20:21], v[24:25]
	v_pk_mul_f32 v[26:27], v[16:17], v[26:27]
	global_store_dwordx4 v[32:33], v[24:27], off offset:2048 sc1
	v_pk_mul_f32 v[20:21], v[22:23], v[18:19] op_sel_hi:[1,0]
	v_pk_mul_f32 v[18:19], v[14:15], v[18:19] op_sel_hi:[1,0]
	s_nop 1
	v_mov_b64_e32 v[14:15], v[228:229]
	v_mov_b64_e32 v[16:17], v[230:231]
	v_pk_mul_f32 v[14:15], v[18:19], v[14:15]
	v_pk_mul_f32 v[16:17], v[20:21], v[16:17]
	global_store_dwordx4 v[32:33], v[14:17], off offset:3072 sc1
	s_branch .LBB0_1632
